# speedup vs baseline: 1.0350x; 1.0012x over previous
.Lfarslow_pre:
	s_waitcnt lgkmcnt(0)
	v_sub_u32_e32 v165, v137, v116
	v_mul_u32_u24_e32 v165, 3, v165
	v_add_u32_e32 v165, v0, v165
	v_add_u32_e32 v165, 32, v165
	ds_read_b64 v[64:65], v165
	v_and_b32_e32 v164, 0x3ff, v38
	v_mov_b64_e32 v[166:167], v[158:159]
	s_movk_i32 s22, 24
	s_waitcnt lgkmcnt(0)

.Lfarslow_A:
	s_waitcnt lgkmcnt(0)
	v_sub_u32_e32 v165, v137, v116
	v_mul_u32_u24_e32 v165, 3, v165
	v_add_u32_e32 v165, v0, v165
	v_add_u32_e32 v165, -1504, v165
	ds_read_b64 v[64:65], v165
	v_and_b32_e32 v164, 0x3ff, v46
	v_mov_b64_e32 v[166:167], v[158:159]
	s_movk_i32 s22, 24
	s_waitcnt lgkmcnt(0)

.Lfarslow_B:
	s_waitcnt lgkmcnt(0)
	v_sub_u32_e32 v165, v172, v116
	v_mul_u32_u24_e32 v165, 3, v165
	v_add_u32_e32 v165, v0, v165
	v_add_u32_e32 v165, -1504, v165
	ds_read_b64 v[64:65], v165
	v_and_b32_e32 v164, 0x3ff, v38
	v_mov_b64_e32 v[166:167], v[158:159]
	s_movk_i32 s22, 24
	s_waitcnt lgkmcnt(0)
